# v29 + route phase router-weight LDS fill with 8 loads in flight
# speedup vs baseline: 1.0170x; 1.0003x over previous
; #define GAS __attribute__((address_space(1)))
; __device__ __forceinline__ void route_phase(Frame& F) {
;     ...
;     for (int s4 = F.tid; s4 < 4096; s4 += 512) { const int k = s4 >> 1, half = s4 & 1, j = k >> 8, ln = (k >> 2) & 63, q = k & 3;
;         rwl[((j * 4 + q) * 2 + half) * 64 + ln] = *(const GAS f32x4*)(rw + (size_t)k * 8 + 4 * half); }
.LBB0_1738:
	v_add_u32_e32 v12, 0x0, v4
	v_ashrrev_i32_e32 v10, 1, v12
	v_ashrrev_i32_e32 v11, 31, v10
	v_lshlrev_b64 v[10:11], 5, v[10:11]
	v_lshl_add_u64 v[10:11], v[2:3], 0, v[10:11]
	global_load_dwordx4 v[200:203], v[10:11], off
	v_add_u32_e32 v12, 0x200, v4
	v_ashrrev_i32_e32 v10, 1, v12
	v_ashrrev_i32_e32 v11, 31, v10
	v_lshlrev_b64 v[10:11], 5, v[10:11]
	v_lshl_add_u64 v[10:11], v[2:3], 0, v[10:11]
	global_load_dwordx4 v[204:207], v[10:11], off
	v_add_u32_e32 v12, 0x400, v4
	v_ashrrev_i32_e32 v10, 1, v12
	v_ashrrev_i32_e32 v11, 31, v10
	v_lshlrev_b64 v[10:11], 5, v[10:11]
	v_lshl_add_u64 v[10:11], v[2:3], 0, v[10:11]
	global_load_dwordx4 v[208:211], v[10:11], off
	v_add_u32_e32 v12, 0x600, v4
	v_ashrrev_i32_e32 v10, 1, v12
	v_ashrrev_i32_e32 v11, 31, v10
	v_lshlrev_b64 v[10:11], 5, v[10:11]
	v_lshl_add_u64 v[10:11], v[2:3], 0, v[10:11]
	global_load_dwordx4 v[212:215], v[10:11], off
	v_add_u32_e32 v12, 0x800, v4
	v_ashrrev_i32_e32 v10, 1, v12
	v_ashrrev_i32_e32 v11, 31, v10
	v_lshlrev_b64 v[10:11], 5, v[10:11]
	v_lshl_add_u64 v[10:11], v[2:3], 0, v[10:11]
	global_load_dwordx4 v[216:219], v[10:11], off
	v_add_u32_e32 v12, 0xa00, v4
	v_ashrrev_i32_e32 v10, 1, v12
	v_ashrrev_i32_e32 v11, 31, v10
	v_lshlrev_b64 v[10:11], 5, v[10:11]
	v_lshl_add_u64 v[10:11], v[2:3], 0, v[10:11]
	global_load_dwordx4 v[220:223], v[10:11], off
	v_add_u32_e32 v12, 0xc00, v4
	v_ashrrev_i32_e32 v10, 1, v12
	v_ashrrev_i32_e32 v11, 31, v10
	v_lshlrev_b64 v[10:11], 5, v[10:11]
	v_lshl_add_u64 v[10:11], v[2:3], 0, v[10:11]
	global_load_dwordx4 v[224:227], v[10:11], off
	v_add_u32_e32 v12, 0xe00, v4
	v_ashrrev_i32_e32 v10, 1, v12
	v_ashrrev_i32_e32 v11, 31, v10
	v_lshlrev_b64 v[10:11], 5, v[10:11]
	v_lshl_add_u64 v[10:11], v[2:3], 0, v[10:11]
	global_load_dwordx4 v[228:231], v[10:11], off
	v_add_u32_e32 v12, 0x0, v4
	v_ashrrev_i32_e32 v10, 1, v12
	v_and_b32_e32 v5, 0xffffe00, v12
	v_lshlrev_b32_e32 v10, 11, v10
	v_lshlrev_b32_e32 v11, 1, v12
	v_lshlrev_b32_e32 v5, 4, v5
	v_and_b32_e32 v10, 0x1800, v10
	v_and_b32_e32 v11, 0x3f0, v11
	v_add3_u32 v5, 0, v5, v10
	v_add3_u32 v5, v5, v1, v11
	s_waitcnt vmcnt(7)
	ds_write_b128 v5, v[200:203] offset:2048
	v_add_u32_e32 v12, 0x200, v4
	v_ashrrev_i32_e32 v10, 1, v12
	v_and_b32_e32 v5, 0xffffe00, v12
	v_lshlrev_b32_e32 v10, 11, v10
	v_lshlrev_b32_e32 v11, 1, v12
	v_lshlrev_b32_e32 v5, 4, v5
	v_and_b32_e32 v10, 0x1800, v10
	v_and_b32_e32 v11, 0x3f0, v11
	v_add3_u32 v5, 0, v5, v10
	v_add3_u32 v5, v5, v1, v11
	s_waitcnt vmcnt(6)
	ds_write_b128 v5, v[204:207] offset:2048
	v_add_u32_e32 v12, 0x400, v4
	v_ashrrev_i32_e32 v10, 1, v12
	v_and_b32_e32 v5, 0xffffe00, v12
	v_lshlrev_b32_e32 v10, 11, v10
	v_lshlrev_b32_e32 v11, 1, v12
	v_lshlrev_b32_e32 v5, 4, v5
	v_and_b32_e32 v10, 0x1800, v10
	v_and_b32_e32 v11, 0x3f0, v11
	v_add3_u32 v5, 0, v5, v10
	v_add3_u32 v5, v5, v1, v11
	s_waitcnt vmcnt(5)
	ds_write_b128 v5, v[208:211] offset:2048
	v_add_u32_e32 v12, 0x600, v4
	v_ashrrev_i32_e32 v10, 1, v12
	v_and_b32_e32 v5, 0xffffe00, v12
	v_lshlrev_b32_e32 v10, 11, v10
	v_lshlrev_b32_e32 v11, 1, v12
	v_lshlrev_b32_e32 v5, 4, v5
	v_and_b32_e32 v10, 0x1800, v10
	v_and_b32_e32 v11, 0x3f0, v11
	v_add3_u32 v5, 0, v5, v10
	v_add3_u32 v5, v5, v1, v11
	s_waitcnt vmcnt(4)
	ds_write_b128 v5, v[212:215] offset:2048
	v_add_u32_e32 v12, 0x800, v4
	v_ashrrev_i32_e32 v10, 1, v12
	v_and_b32_e32 v5, 0xffffe00, v12
	v_lshlrev_b32_e32 v10, 11, v10
	v_lshlrev_b32_e32 v11, 1, v12
	v_lshlrev_b32_e32 v5, 4, v5
	v_and_b32_e32 v10, 0x1800, v10
	v_and_b32_e32 v11, 0x3f0, v11
	v_add3_u32 v5, 0, v5, v10
	v_add3_u32 v5, v5, v1, v11
	s_waitcnt vmcnt(3)
	ds_write_b128 v5, v[216:219] offset:2048
	v_add_u32_e32 v12, 0xa00, v4
	v_ashrrev_i32_e32 v10, 1, v12
	v_and_b32_e32 v5, 0xffffe00, v12
	v_lshlrev_b32_e32 v10, 11, v10
	v_lshlrev_b32_e32 v11, 1, v12
	v_lshlrev_b32_e32 v5, 4, v5
	v_and_b32_e32 v10, 0x1800, v10
	v_and_b32_e32 v11, 0x3f0, v11
	v_add3_u32 v5, 0, v5, v10
	v_add3_u32 v5, v5, v1, v11
	s_waitcnt vmcnt(2)
	ds_write_b128 v5, v[220:223] offset:2048
	v_add_u32_e32 v12, 0xc00, v4
	v_ashrrev_i32_e32 v10, 1, v12
	v_and_b32_e32 v5, 0xffffe00, v12
	v_lshlrev_b32_e32 v10, 11, v10
	v_lshlrev_b32_e32 v11, 1, v12
	v_lshlrev_b32_e32 v5, 4, v5
	v_and_b32_e32 v10, 0x1800, v10
	v_and_b32_e32 v11, 0x3f0, v11
	v_add3_u32 v5, 0, v5, v10
	v_add3_u32 v5, v5, v1, v11
	s_waitcnt vmcnt(1)
	ds_write_b128 v5, v[224:227] offset:2048
	v_add_u32_e32 v12, 0xe00, v4
	v_ashrrev_i32_e32 v10, 1, v12
	v_and_b32_e32 v5, 0xffffe00, v12
	v_lshlrev_b32_e32 v10, 11, v10
	v_lshlrev_b32_e32 v11, 1, v12
	v_lshlrev_b32_e32 v5, 4, v5
	v_and_b32_e32 v10, 0x1800, v10
	v_and_b32_e32 v11, 0x3f0, v11
	v_add3_u32 v5, 0, v5, v10
	v_add3_u32 v5, v5, v1, v11
	s_waitcnt vmcnt(0)
	ds_write_b128 v5, v[228:231] offset:2048
